# static priority raise (s_setprio 1) for waves 4-7 in the later iteration kernels and k_final
# baseline (speedup 1.0000x reference)
.LBB1_9:
	v_and_b32_e32 v1, 63, v0
	s_lshr_b32 s20, s15, 6
	s_cmp_lt_u32 s20, 4
	s_cbranch_scc1 .Lfin_prio
	s_setprio 1
.Lfin_prio:
	s_andn2_b64 vcc, exec, s[0:1]
	s_mov_b32 s15, 0
	s_cbranch_vccnz .LBB1_36
	s_lshl_b64 s[0:1], s[14:15], 19
	s_add_u32 s0, s18, s0
	s_addc_u32 s1, s19, s1
	v_lshlrev_b32_e32 v18, 4, v143
	v_mov_b32_e32 v19, 0
	v_lshl_add_u64 v[138:139], s[0:1], 0, v[18:19]
	s_lshl_b64 s[0:1], s[16:17], 16
	s_lshl_b32 s14, s20, 2
	s_add_u32 s16, s4, s0
	v_lshlrev_b32_e32 v9, 1, v0
	s_addc_u32 s17, s5, s1
	s_lshr_b32 s0, 0x73261540, s14
	v_and_b32_e32 v5, 19, v0
	v_and_b32_e32 v9, 8, v9
	v_lshrrev_b32_e32 v11, 1, v0
	v_cmp_gt_u32_e64 s[2:3], 32, v1
	s_lshl_b32 s1, s0, 5
	v_or_b32_e32 v10, v9, v5
	v_and_b32_e32 v11, 4, v11
	v_lshlrev_b32_e32 v2, 2, v0
	s_and_b32 s1, s1, 0xe0
	v_and_b32_e32 v3, 32, v0
	v_add_u32_e32 v149, 0x23900, v2
	v_exp_f32_e32 v150, 0xc0b8aa2f
	v_or_b32_e32 v151, 0x20800, v2
	s_xor_b32 s21, s1, 0xff
	v_or3_b32 v152, v10, v11, s1
	v_lshl_or_b32 v4, s1, 2, v3
	v_or_b32_e32 v154, 0x22000, v2
	v_or3_b32 v2, v5, s1, v9
	s_movk_i32 s1, 0x100
	s_and_b32 s0, s0, 7
	v_or3_b32 v155, v2, v11, s1
	v_lshl_or_b32 v2, s0, 7, v3
	v_mov_b32_e32 v18, v19
	v_mov_b32_e32 v32, v19
	v_mov_b32_e32 v33, v19
	v_or_b32_e32 v153, 0x22000, v4
	v_or_b32_e32 v156, 0x20800, v2
	v_mov_b32_e32 v20, v19
	v_mov_b32_e32 v21, v19
	v_mov_b32_e32 v22, v19
	v_mov_b32_e32 v23, v19
	v_mov_b32_e32 v24, v19
	v_mov_b32_e32 v25, v19
	v_mov_b32_e32 v26, v19
	v_mov_b32_e32 v27, v19
	v_mov_b32_e32 v28, v19
	v_mov_b32_e32 v29, v19
	v_mov_b32_e32 v30, v19
	v_mov_b32_e32 v31, v19
	v_mov_b64_e32 v[64:65], v[32:33]
	v_mov_b64_e32 v[80:81], v[32:33]
	v_mov_b64_e32 v[48:49], v[32:33]
	v_mov_b64_e32 v[2:3], v[18:19]
	v_cmp_eq_u32_e64 s[4:5], 0, v1
	s_add_i32 s14, s14, 0x23a00
	v_or_b32_e32 v142, 0x200, v0
	v_or_b32_e32 v141, 0x400, v0
	v_mov_b32_e32 v157, 0x23a00
	v_mov_b32_e32 v158, 0x23a10
	s_mov_b32 s22, 0x44800000
	v_mov_b32_e32 v159, 0xff800000
	v_mov_b64_e32 v[62:63], v[30:31]
	v_mov_b64_e32 v[60:61], v[28:29]
	v_mov_b64_e32 v[58:59], v[26:27]
	v_mov_b64_e32 v[56:57], v[24:25]
	v_mov_b64_e32 v[54:55], v[22:23]
	v_mov_b64_e32 v[52:53], v[20:21]
	v_mov_b64_e32 v[50:51], v[18:19]
	v_mov_b64_e32 v[78:79], v[30:31]
	v_mov_b64_e32 v[76:77], v[28:29]
	v_mov_b64_e32 v[74:75], v[26:27]
	v_mov_b64_e32 v[72:73], v[24:25]
	v_mov_b64_e32 v[70:71], v[22:23]
	v_mov_b64_e32 v[68:69], v[20:21]
	v_mov_b64_e32 v[66:67], v[18:19]
	v_mov_b64_e32 v[46:47], v[30:31]
	v_mov_b64_e32 v[44:45], v[28:29]
	v_mov_b64_e32 v[42:43], v[26:27]
	v_mov_b64_e32 v[40:41], v[24:25]
	v_mov_b64_e32 v[38:39], v[22:23]
	v_mov_b64_e32 v[36:37], v[20:21]
	v_mov_b64_e32 v[34:35], v[18:19]
	v_mov_b64_e32 v[4:5], v[20:21]
	v_mov_b64_e32 v[6:7], v[22:23]
	v_mov_b64_e32 v[8:9], v[24:25]
	v_mov_b64_e32 v[10:11], v[26:27]
	v_mov_b64_e32 v[12:13], v[28:29]
	v_mov_b64_e32 v[14:15], v[30:31]
	v_mov_b64_e32 v[16:17], v[32:33]
	v_mov_b32_e32 v32, 0
	s_cmp_eq_u32 s15, 0
	s_cselect_b64 s[0:1], -1, 0
	s_and_b64 vcc, exec, s[0:1]
	s_cbranch_vccnz .LBB1_12

_Z6k_iterILb0ELb0EEvPKfS1_PKiPK15HIP_vector_typeIfLj4EES7_S1_S1_S3_S1_PfS8_S1_S3_PDF16_PS5_SA_PiSA_SB_:
	s_and_b32 s38, s0, 0xfffff000
	s_mov_b32 s39, s1
	s_load_dwordx2 s[8:9], s[0:1], 0x80
	s_load_dwordx4 s[4:7], s[0:1], 0x70
	s_load_dwordx4 s[16:19], s[0:1], 0x40
	v_readfirstlane_b32 s12, v0
	v_cmp_gt_u32_e64 s[14:15], 64, v0
	v_lshlrev_b32_e32 v1, 2, v0
	s_and_saveexec_b64 s[10:11], s[14:15]
	v_mov_b32_e32 v2, 0
	ds_write_b32 v1, v2 offset:5152
	s_or_b64 exec, exec, s[10:11]
	s_lshl_b32 s3, s2, 5
	s_and_b32 s3, s3, 0xe0
	s_lshr_b32 s2, s2, 3
	s_add_i32 s2, s3, s2
	s_lshl_b32 s25, s2, 6
	v_and_b32_e32 v2, 31, v0
	v_or_b32_e32 v4, s25, v2
	v_mov_b32_e32 v5, 0
	s_lshr_b32 s27, s12, 6
	s_lshl_b32 s32, s27, 2
	s_lshr_b32 s32, 0x73261540, s32
	s_lshl_b32 s32, s32, 5
	s_and_b32 s32, s32, 0xe0
	s_cmp_lt_u32 s27, 4
	s_cbranch_scc1 .Lffc_prio
	s_setprio 1
.Lffc_prio:
	v_or_b32_e32 v176, s32, v2
	v_lshlrev_b32_e32 v177, 4, v176
	v_add_u32_e32 v178, 0x1000, v177
	v_add_u32_e32 v179, 0x2000, v177
	v_add_u32_e32 v180, 0x3000, v177
	v_add_u32_e32 v181, 0x4000, v177
	v_add_u32_e32 v182, 0x5000, v177
	s_mov_b32 s3, 0
	s_lshl_b64 s[34:35], s[2:3], 16
	s_lshl_b32 s33, s2, 2
	s_waitcnt lgkmcnt(0)
	s_load_dword s24, s[8:9], s33 offset:0x0
	s_add_u32 s20, s4, s34
	s_addc_u32 s21, s5, s35
	v_lshl_add_u64 v[4:5], v[4:5], 4, s[6:7]
	global_load_dwordx3 v[30:32], v[4:5], off
	global_load_dwordx3 v[26:28], v[4:5], off offset:512
	global_load_dwordx4 v[2:5], v177, s[20:21]
	global_load_dwordx4 v[6:9], v178, s[20:21]
	global_load_dwordx4 v[10:13], v179, s[20:21]
	global_load_dwordx4 v[14:17], v180, s[20:21]
	global_load_dwordx4 v[18:21], v181, s[20:21]
	global_load_dwordx4 v[22:25], v182, s[20:21]
	s_cmp_eq_u32 s27, 0
	s_cbranch_scc1 .Lffc_touch_14
	s_cmp_eq_u32 s27, 1
	s_cbranch_scc1 .Lffc_touch_19
	s_cmp_eq_u32 s27, 2
	s_cbranch_scc1 .Lffc_touch_11
	s_cmp_eq_u32 s27, 3
	s_cbranch_scc1 .Lffc_touch_15
	s_cmp_eq_u32 s27, 4
	s_cbranch_scc1 .Lffc_touch_31
	s_cmp_eq_u32 s27, 5
	s_cbranch_scc1 .Lffc_touch_37
	s_cmp_eq_u32 s27, 6
	s_cbranch_scc1 .Lffc_touch_39

_Z6k_iterILb0ELb1EEvPKfS1_PKiPK15HIP_vector_typeIfLj4EES7_S1_S1_S3_S1_PfS8_S1_S3_PDF16_PS5_SA_PiSA_SB_:
	s_and_b32 s38, s0, 0xfffff000
	s_mov_b32 s39, s1
	s_load_dwordx2 s[8:9], s[0:1], 0x80
	s_load_dwordx4 s[4:7], s[0:1], 0x70
	s_load_dwordx4 s[16:19], s[0:1], 0x40
	s_load_dwordx2 s[22:23], s[0:1], 0x50
	s_load_dwordx2 s[42:43], s[0:1], 0x88
	v_readfirstlane_b32 s12, v0
	v_cmp_gt_u32_e64 s[14:15], 64, v0
	v_lshlrev_b32_e32 v1, 2, v0
	s_and_saveexec_b64 s[10:11], s[14:15]
	v_mov_b32_e32 v2, 0
	ds_write_b32 v1, v2 offset:5152
	s_or_b64 exec, exec, s[10:11]
	s_lshl_b32 s3, s2, 5
	s_and_b32 s3, s3, 0xe0
	s_lshr_b32 s2, s2, 3
	s_add_i32 s2, s3, s2
	s_lshl_b32 s29, s2, 6
	v_and_b32_e32 v2, 31, v0
	v_or_b32_e32 v4, s29, v2
	v_mov_b32_e32 v5, 0
	s_lshr_b32 s30, s12, 6
	s_lshl_b32 s32, s30, 2
	s_lshr_b32 s32, 0x73261540, s32
	s_lshl_b32 s32, s32, 5
	s_and_b32 s32, s32, 0xe0
	s_cmp_lt_u32 s30, 4
	s_cbranch_scc1 .Lftc_prio
	s_setprio 1
.Lftc_prio:
	v_or_b32_e32 v176, s32, v2
	v_lshlrev_b32_e32 v177, 4, v176
	v_add_u32_e32 v178, 0x1000, v177
	v_add_u32_e32 v179, 0x2000, v177
	v_add_u32_e32 v180, 0x3000, v177
	v_add_u32_e32 v181, 0x4000, v177
	v_add_u32_e32 v182, 0x5000, v177
	s_mov_b32 s3, 0
	s_lshl_b64 s[34:35], s[2:3], 16
	s_lshl_b32 s33, s2, 2
	s_waitcnt lgkmcnt(0)
	s_load_dword s26, s[8:9], s33 offset:0x0
	s_add_u32 s20, s4, s34
	s_addc_u32 s21, s5, s35
	v_lshl_add_u64 v[4:5], v[4:5], 4, s[6:7]
	global_load_dwordx3 v[30:32], v[4:5], off
	global_load_dwordx3 v[26:28], v[4:5], off offset:512
	global_load_dwordx4 v[2:5], v177, s[20:21]
	global_load_dwordx4 v[6:9], v178, s[20:21]
	global_load_dwordx4 v[10:13], v179, s[20:21]
	global_load_dwordx4 v[14:17], v180, s[20:21]
	global_load_dwordx4 v[18:21], v181, s[20:21]
	global_load_dwordx4 v[22:25], v182, s[20:21]
	s_cmp_eq_u32 s30, 0
	s_cbranch_scc1 .Lftc_touch_14
	s_cmp_eq_u32 s30, 1
	s_cbranch_scc1 .Lftc_touch_19
	s_cmp_eq_u32 s30, 2
	s_cbranch_scc1 .Lftc_touch_11
	s_cmp_eq_u32 s30, 3
	s_cbranch_scc1 .Lftc_touch_15
	s_cmp_eq_u32 s30, 4
	s_cbranch_scc1 .Lftc_touch_31
	s_cmp_eq_u32 s30, 5
	s_cbranch_scc1 .Lftc_touch_37
	s_cmp_eq_u32 s30, 6
	s_cbranch_scc1 .Lftc_touch_39

.LBB4_39:
	s_waitcnt vmcnt(5)
	v_rcp_f32_e32 v2, v133
	s_waitcnt vmcnt(4)
	v_rcp_f32_e32 v3, v132
	s_waitcnt vmcnt(3)
	v_rcp_f32_e32 v4, v131
	v_cmp_lt_f32_e32 vcc, 0, v133
	s_waitcnt vmcnt(2)
	v_rcp_f32_e32 v5, v130
	s_waitcnt vmcnt(1)
	v_rcp_f32_e32 v6, v129
	v_cndmask_b32_e32 v2, 0, v2, vcc
	v_cmp_lt_f32_e32 vcc, 0, v132
	s_waitcnt vmcnt(0)
	v_rcp_f32_e32 v7, v128
	s_getpc_b64 s[36:37]
	s_sub_u32 s36, s36, 0x9644
	s_subb_u32 s37, s37, 0
	v_lshlrev_b32_e32 v183, 6, v0
	v_min_u32_e32 v183, 0x1d80, v183
	global_load_dword v183, v183, s[36:37]
	v_lshlrev_b32_e32 v182, 6, v38
	global_load_dword v182, v182, s[38:39]
	s_lshl_b32 s40, s29, 10
	s_add_u32 s40, s42, s40
	s_addc_u32 s41, s43, 0
	v_lshlrev_b32_e32 v181, 6, v0
	v_and_b32_e32 v181, 0x7fc0, v181
	global_load_dword v181, v181, s[40:41]
	s_mov_b32 s4, 0x42c80000
	v_cndmask_b32_e32 v3, 0, v3, vcc
	v_cmp_lt_f32_e32 vcc, 0, v131
	v_cmp_ngt_f32_e64 s[2:3], s4, v3
	s_mov_b64 s[6:7], 0
	v_cndmask_b32_e32 v4, 0, v4, vcc
	v_cmp_lt_f32_e32 vcc, 0, v130
	s_nop 1
	v_cndmask_b32_e32 v5, 0, v5, vcc
	v_cmp_lt_f32_e32 vcc, 0, v129
	s_nop 1
	v_cndmask_b32_e32 v6, 0, v6, vcc
	v_cmp_lt_f32_e32 vcc, 0, v128
	s_nop 1
	v_cndmask_b32_e32 v7, 0, v7, vcc
	v_cmp_ngt_f32_e32 vcc, s4, v2
	s_or_b64 s[2:3], vcc, s[2:3]
	v_cmp_ngt_f32_e32 vcc, s4, v4
	s_or_b64 s[2:3], s[2:3], vcc
	v_cmp_ngt_f32_e32 vcc, s4, v5
	s_or_b64 s[2:3], s[2:3], vcc
	v_cmp_ngt_f32_e32 vcc, s4, v6
	s_or_b64 s[2:3], s[2:3], vcc
	v_cmp_ngt_f32_e32 vcc, s4, v7
	s_or_b64 s[2:3], s[2:3], vcc
	v_cndmask_b32_e64 v8, 0, 1, s[2:3]
	v_cmp_ne_u32_e32 vcc, 0, v8
	s_cmp_eq_u64 vcc, 0
	s_cselect_b64 s[2:3], -1, 0
	v_cndmask_b32_e64 v8, 0, 1, s[2:3]
	s_nop 0
	v_readfirstlane_b32 s2, v8
	s_bitcmp0_b32 s2, 0
	s_cbranch_scc0 .LBB4_45
	s_cmp_lt_i32 s28, 4
	s_cbranch_scc1 .LBB4_46
	s_cmp_gt_i32 s28, 4
	s_cbranch_scc0 .LBB4_47
	s_mov_b64 s[4:5], -1
	v_mov_b32_e32 v8, 0
	s_cmp_gt_i32 s28, 5
	v_mov_b32_e32 v167, 0
	v_mov_b32_e32 v166, 0
	v_mov_b32_e32 v165, 0
	v_mov_b32_e32 v164, 0
	v_mov_b32_e32 v162, 0
	v_mov_b32_e32 v160, 0
	v_mov_b32_e32 v159, 0
	v_mov_b32_e32 v157, 0
	v_mov_b32_e32 v151, 0
	v_mov_b32_e32 v149, 0
	v_mov_b32_e32 v147, 0
	v_mov_b32_e32 v146, 0
	v_mov_b32_e32 v144, 0
	v_mov_b32_e32 v143, 0
	v_mov_b32_e32 v152, 0
	v_mov_b32_e32 v153, 0
	v_mov_b32_e32 v154, 0
	v_mov_b32_e32 v155, 0
	v_mov_b32_e32 v156, 0
	v_mov_b32_e32 v158, 0
	v_mov_b32_e32 v161, 0
	v_mov_b32_e32 v163, 0
	v_mov_b32_e32 v168, 0
	v_mov_b32_e32 v169, 0
	v_mov_b32_e32 v170, 0
	v_mov_b32_e32 v171, 0
	v_mov_b32_e32 v172, 0
	v_mov_b32_e32 v173, 0
	v_mov_b32_e32 v174, 0
	v_mov_b32_e32 v145, 0
	v_mov_b32_e32 v148, 0
	v_mov_b32_e32 v150, 0
	s_cbranch_scc0 .LBB4_50
	s_cmp_eq_u32 s28, 6
	s_cbranch_scc0 .LBB4_49
	v_mov_b32_e32 v145, 0
	v_mov_b32_e32 v148, 0
	v_mov_b32_e32 v150, 0
	v_mov_b32_e32 v143, 0
	v_mov_b32_e32 v144, 0
	v_mov_b32_e32 v146, 0
	v_mov_b32_e32 v147, 0
	v_mov_b32_e32 v149, 0
	v_mov_b32_e32 v151, 0
	v_mov_b32_e32 v152, 0
	v_mov_b32_e32 v153, 0
	v_mov_b32_e32 v154, 0
	v_mov_b32_e32 v155, 0
	v_mov_b32_e32 v156, 0
	v_mov_b32_e32 v158, 0
	v_mov_b32_e32 v161, 0
	v_mov_b32_e32 v163, 0
	v_mov_b32_e32 v157, 0
	v_mov_b32_e32 v159, 0
	v_mov_b32_e32 v160, 0
	v_mov_b32_e32 v162, 0
	v_mov_b32_e32 v164, 0
	v_mov_b32_e32 v165, 0
	v_mov_b32_e32 v166, 0
	v_mov_b32_e32 v167, 0
	v_mov_b32_e32 v168, 0
	v_mov_b32_e32 v169, 0
	v_mov_b32_e32 v170, 0
	v_mov_b32_e32 v171, 0
	v_mov_b32_e32 v172, 0
	v_mov_b32_e32 v173, 0
	v_mov_b32_e32 v174, 0
	v_fma_mix_f32 v148, v43, v7, v148 op_sel_hi:[1,0,0]
	v_fma_mix_f32 v150, v45, v7, v150 op_sel_hi:[1,0,0]
	v_fma_mix_f32 v143, v50, v7, v143 op_sel_hi:[1,0,0]
	v_fma_mix_f32 v144, v54, v7, v144 op_sel_hi:[1,0,0]
	v_fma_mix_f32 v146, v58, v7, v146 op_sel_hi:[1,0,0]
	v_fma_mix_f32 v147, v61, v7, v147 op_sel_hi:[1,0,0]
	v_fma_mix_f32 v149, v64, v7, v149 op_sel_hi:[1,0,0]
	v_fma_mix_f32 v151, v66, v7, v151 op_sel_hi:[1,0,0]
	v_fma_mix_f32 v152, v43, v7, v152 op_sel:[1,0,0] op_sel_hi:[1,0,0]
	v_fma_mix_f32 v153, v45, v7, v153 op_sel:[1,0,0] op_sel_hi:[1,0,0]
	v_fma_mix_f32 v154, v50, v7, v154 op_sel:[1,0,0] op_sel_hi:[1,0,0]
	v_fma_mix_f32 v155, v54, v7, v155 op_sel:[1,0,0] op_sel_hi:[1,0,0]
	v_fma_mix_f32 v156, v58, v7, v156 op_sel:[1,0,0] op_sel_hi:[1,0,0]
	v_fma_mix_f32 v158, v61, v7, v158 op_sel:[1,0,0] op_sel_hi:[1,0,0]
	v_fma_mix_f32 v161, v64, v7, v161 op_sel:[1,0,0] op_sel_hi:[1,0,0]
	v_fma_mix_f32 v163, v66, v7, v163 op_sel:[1,0,0] op_sel_hi:[1,0,0]
	v_fma_mix_f32 v157, v72, v7, v157 op_sel_hi:[1,0,0]
	v_fma_mix_f32 v159, v76, v7, v159 op_sel_hi:[1,0,0]
	v_fma_mix_f32 v160, v83, v7, v160 op_sel_hi:[1,0,0]
	v_fma_mix_f32 v162, v85, v7, v162 op_sel_hi:[1,0,0]
	v_fma_mix_f32 v164, v89, v7, v164 op_sel_hi:[1,0,0]
	v_fma_mix_f32 v165, v92, v7, v165 op_sel_hi:[1,0,0]
	v_fma_mix_f32 v166, v95, v7, v166 op_sel_hi:[1,0,0]
	v_fma_mix_f32 v167, v96, v7, v167 op_sel_hi:[1,0,0]
	v_fma_mix_f32 v168, v72, v7, v168 op_sel:[1,0,0] op_sel_hi:[1,0,0]
	v_fma_mix_f32 v169, v76, v7, v169 op_sel:[1,0,0] op_sel_hi:[1,0,0]
	v_fma_mix_f32 v170, v83, v7, v170 op_sel:[1,0,0] op_sel_hi:[1,0,0]
	v_fma_mix_f32 v171, v85, v7, v171 op_sel:[1,0,0] op_sel_hi:[1,0,0]
	v_fma_mix_f32 v172, v89, v7, v172 op_sel:[1,0,0] op_sel_hi:[1,0,0]
	v_fma_mix_f32 v173, v92, v7, v173 op_sel:[1,0,0] op_sel_hi:[1,0,0]
	v_fma_mix_f32 v174, v95, v7, v174 op_sel:[1,0,0] op_sel_hi:[1,0,0]
	v_fma_mix_f32 v145, v96, v7, v145 op_sel:[1,0,0] op_sel_hi:[1,0,0]
	s_branch .LBB4_50
